# all expert weight conversion of layers 1-3 moved from the prologue into the grid barriers (waves 1-7, one item per barrier)
# speedup vs baseline: 1.0118x; 1.0118x over previous
.LBB0_133:
	s_add_i32 s46, s41, s33
	s_add_i32 s2, s46, 0xffff8ea0
	s_cmp_lt_i32 s2, 0
	s_cbranch_scc1 .Lp0_noskip
	s_cmp_lt_i32 s2, 0x6000
	s_cbranch_scc1 .Lp0_skip
	s_add_i32 s2, s2, 0xffff9750
	s_cmp_lt_i32 s2, 0
	s_cbranch_scc1 .Lp0_noskip
	s_cmp_lt_i32 s2, 0x6000
	s_cbranch_scc1 .Lp0_skip
	s_add_i32 s2, s2, 0xffff9750
	s_cmp_lt_i32 s2, 0
	s_cbranch_scc1 .Lp0_noskip
	s_cmp_lt_i32 s2, 0x6000
	s_cbranch_scc0 .Lp0_noskip
.Lp0_skip:
	s_add_i32 s46, s46, 0x6000
.Lp0_noskip:
	s_cmp_lt_i32 s46, 0x1a2c0
	s_cselect_b64 s[14:15], -1, 0
	s_cmp_gt_i32 s46, 0x1a2bf
	s_cselect_b64 s[2:3], -1, 0
	s_and_b64 vcc, exec, s[2:3]
	v_mov_b32_e32 v154, v137
	s_mov_b64 s[16:17], s[10:11]
	s_mov_b32 s49, s26
	s_mov_b32 s47, s24
	s_mov_b32 s48, s25
	s_cbranch_vccnz .LBB0_175
	s_mul_hi_i32 s8, s46, 0x4e407f29
	s_lshr_b32 s9, s8, 31
	s_ashr_i32 s8, s8, 13
	s_add_i32 s8, s8, s9
	s_mul_i32 s51, s8, 0xffff9750
	s_add_i32 s51, s51, s46
	s_cmpk_gt_i32 s51, 0x5bf
	s_cbranch_scc0 .LBB0_156
	s_cmpk_gt_u32 s51, 0x5ef
	s_mov_b64 s[22:23], -1
	s_cbranch_scc0 .LBB0_153
	s_cmpk_gt_u32 s51, 0x62f
	s_cbranch_scc0 .LBB0_150
	s_cmpk_gt_u32 s51, 0x7af
	s_cbranch_scc0 .LBB0_147
	s_cmpk_gt_u32 s51, 0x8af
	s_cbranch_scc0 .LBB0_144
	s_add_i32 s9, s51, 0xfffff750
	s_mul_hi_u32 s12, s9, 0xaaaaaaab
	s_lshr_b32 s12, s12, 9
	s_mul_i32 s48, s12, 0xfffffd00
	s_add_i32 s48, s48, s9
	s_cmpk_gt_i32 s48, 0x1ff
	s_cbranch_scc0 .LBB0_141
	s_add_i32 s16, s48, 0xfffffe00
	s_lshr_b32 s52, s16, 5
	s_mov_b64 s[16:17], s[0:1]
	s_and_b32 s47, s9, 31
	s_load_dwordx2 s[16:17], s[16:17], 0xe8
	s_ashr_i32 s9, s8, 31
	s_lshl_b64 s[18:19], s[12:13], 20
	s_lshl_b64 s[20:21], s[8:9], 25
	s_add_u32 s20, s18, s20
	s_addc_u32 s21, s19, s21
	s_lshl_b64 s[18:19], s[20:21], 2
	s_waitcnt lgkmcnt(0)
	s_add_u32 s18, s16, s18
	s_addc_u32 s19, s17, s19
	s_add_u32 s16, s27, s20
	s_addc_u32 s17, s28, s21
	s_mov_b64 s[22:23], 0

.Lcvt_site_0:
	s_mul_i32 s30, s62, 11
	s_add_i32 s30, s30, 1
	s_mov_b32 s31, 0
	s_branch .Lcvtw
.Lcvt_site_1:
	s_mul_i32 s30, s62, 11
	s_add_i32 s30, s30, 2
	s_mov_b32 s31, 1
	s_branch .Lcvtw
.Lcvt_site_2:
	s_mul_i32 s30, s62, 11
	s_add_i32 s30, s30, 3
	s_mov_b32 s31, 2
	s_branch .Lcvtw
.Lcvt_site_3:
	s_mul_i32 s30, s62, 11
	s_add_i32 s30, s30, 4
	s_mov_b32 s31, 3
	s_branch .Lcvtw
.Lcvt_site_4:
	s_mul_i32 s30, s62, 11
	s_add_i32 s30, s30, 5
	s_mov_b32 s31, 4
	s_branch .Lcvtw
.Lcvt_site_5:
	s_mul_i32 s30, s62, 11
	s_add_i32 s30, s30, 6
	s_mov_b32 s31, 5
	s_branch .Lcvtw
.Lcvt_site_6:
	s_mul_i32 s30, s62, 11
	s_add_i32 s30, s30, 7
	s_mov_b32 s31, 6
	s_branch .Lcvtw
.Lcvt_site_7:
	s_mul_i32 s30, s62, 11
	s_add_i32 s30, s30, 8
	s_mov_b32 s31, 7
	s_branch .Lcvtw
.Lcvt_site_8:
	s_mul_i32 s30, s62, 11
	s_add_i32 s30, s30, 9
	s_mov_b32 s31, 8
	s_branch .Lcvtw
.Lcvt_site_9:
	s_mul_i32 s30, s62, 11
	s_add_i32 s30, s30, 10
	s_mov_b32 s31, 9
	s_branch .Lcvtw
.Lcvt_site_10:
	s_mul_i32 s30, s62, 11
	s_add_i32 s30, s30, 11
	s_mov_b32 s31, 10
	s_branch .Lcvtw
.Lcvt_site_11:
	s_mov_b32 s30, 0
	s_mov_b32 s31, 11
	s_branch .Lcvtw
.Lcvtw:
	s_mov_b64 exec, -1
	v_lshrrev_b32_e32 v2, 6, v0
	v_and_b32_e32 v3, 63, v0
	s_nop 0
	v_readfirstlane_b32 s4, v2
	s_nop 3
	s_mul_i32 s5, s80, 7
	s_add_i32 s5, s5, s4
	s_add_i32 s5, s5, -1
	s_mul_i32 s6, s30, 0x700
	s_add_i32 s5, s5, s6
	s_cmp_ge_u32 s5, 0x12000
	s_cbranch_scc1 .Lcvtw_ret
	s_mov_b32 s6, 1
	s_cmp_ge_u32 s5, 0x6000
	s_cbranch_scc0 .Lcvtw_l
	s_add_i32 s5, s5, 0xffffa000
	s_mov_b32 s6, 2
	s_cmp_ge_u32 s5, 0x6000
	s_cbranch_scc0 .Lcvtw_l
	s_add_i32 s5, s5, 0xffffa000
	s_mov_b32 s6, 3
.Lcvtw_l:
	s_lshr_b32 s7, s5, 8
	s_mul_i32 s7, s7, 0xaaab
	s_lshr_b32 s7, s7, 17
	s_mul_i32 s8, s7, 0x300
	s_sub_i32 s8, s5, s8
	s_lshl_b32 s9, s6, 5
	s_add_i32 s9, s9, s7
	s_load_dwordx2 s[2:3], s[0:1], 0x100
	s_cmp_lt_u32 s8, 0x200
	s_cbranch_scc0 .Lcvtw_dn
	s_load_dwordx2 s[10:11], s[0:1], 0xd8
	s_lshr_b32 s12, s8, 6
	s_and_b32 s13, s8, 63
	s_lshr_b32 s14, s13, 2
	s_and_b32 s14, s14, 7
	s_lshl_b32 s14, s14, 3
	s_and_b32 s15, s13, 3
	s_add_i32 s14, s14, s15
	s_lshr_b32 s15, s13, 5
	s_lshl_b32 s15, s15, 2
	s_add_i32 s14, s14, s15
	s_mov_b32 s16, 13
	s_mov_b32 s18, s9
	s_mov_b32 s19, 0
	s_lshl_b64 s[20:21], s[18:19], 23
	s_lshl_b64 s[22:23], s[18:19], 21
	s_mov_b32 s24, 0x6000000
	s_branch .Lcvtw_common
.Lcvtw_dn:
	s_load_dwordx2 s[10:11], s[0:1], 0xe8
	s_add_i32 s8, s8, 0xfffffe00
	s_lshr_b32 s12, s8, 5
	s_and_b32 s13, s8, 31
	s_mov_b32 s14, s13
	s_mov_b32 s16, 12
	s_mov_b32 s18, s9
	s_mov_b32 s19, 0
	s_lshl_b64 s[20:21], s[18:19], 22
	s_lshl_b64 s[22:23], s[18:19], 20
	s_mov_b32 s24, 0x26000000
.Lcvtw_common:
	v_lshrrev_b32_e32 v4, 3, v3
	v_and_b32_e32 v5, 7, v3
	v_lshlrev_b32_e32 v6, s16, v4
	v_lshl_add_u32 v6, v5, 4, v6
	v_mul_u32_u24_e32 v7, 17, v4
	v_and_b32_e32 v8, 3, v3
	v_lshl_add_u32 v7, v8, 2, v7
	v_lshlrev_b32_e32 v7, 2, v7
	v_mul_u32_u24_e32 v8, 0x110, v5
	v_add_lshl_u32 v8, v8, v4, 2
	s_mul_i32 s25, s4, 0x2200
	v_add_u32_e32 v7, s25, v7
	v_add_u32_e32 v8, s25, v8
	v_lshlrev_b32_e32 v9, 10, v4
	v_lshl_add_u32 v9, v5, 4, v9
	v_add_u32_e32 v10, 0x2000, v9
	s_waitcnt lgkmcnt(0)
	s_add_u32 s10, s10, s20
	s_addc_u32 s11, s11, s21
	s_add_i32 s26, s16, 7
	s_lshl_b32 s27, s12, s26
	s_add_u32 s10, s10, s27
	s_addc_u32 s11, s11, 0
	s_lshl_b32 s27, s13, 7
	s_add_u32 s10, s10, s27
	s_addc_u32 s11, s11, 0
	s_add_i32 s26, s16, 3
	s_lshl_b32 s27, 1, s26
	global_load_dwordx4 v[16:19], v6, s[10:11] nt
	s_add_u32 s10, s10, s27
	s_addc_u32 s11, s11, 0
	global_load_dwordx4 v[20:23], v6, s[10:11] nt
	s_add_u32 s10, s10, s27
	s_addc_u32 s11, s11, 0
	global_load_dwordx4 v[24:27], v6, s[10:11] nt
	s_add_u32 s10, s10, s27
	s_addc_u32 s11, s11, 0
	global_load_dwordx4 v[28:31], v6, s[10:11] nt
	s_add_u32 s10, s10, s27
	s_addc_u32 s11, s11, 0
	global_load_dwordx4 v[32:35], v6, s[10:11] nt
	s_add_u32 s10, s10, s27
	s_addc_u32 s11, s11, 0
	global_load_dwordx4 v[36:39], v6, s[10:11] nt
	s_add_u32 s10, s10, s27
	s_addc_u32 s11, s11, 0
	global_load_dwordx4 v[40:43], v6, s[10:11] nt
	s_add_u32 s10, s10, s27
	s_addc_u32 s11, s11, 0
	global_load_dwordx4 v[44:47], v6, s[10:11] nt
	s_add_u32 s10, s10, s27
	s_addc_u32 s11, s11, 0
	global_load_dwordx4 v[48:51], v6, s[10:11] nt
	s_add_u32 s10, s10, s27
	s_addc_u32 s11, s11, 0
	global_load_dwordx4 v[52:55], v6, s[10:11] nt
	s_add_u32 s10, s10, s27
	s_addc_u32 s11, s11, 0
	global_load_dwordx4 v[56:59], v6, s[10:11] nt
	s_add_u32 s10, s10, s27
	s_addc_u32 s11, s11, 0
	global_load_dwordx4 v[60:63], v6, s[10:11] nt
	s_add_u32 s10, s10, s27
	s_addc_u32 s11, s11, 0
	global_load_dwordx4 v[64:67], v6, s[10:11] nt
	s_add_u32 s10, s10, s27
	s_addc_u32 s11, s11, 0
	global_load_dwordx4 v[68:71], v6, s[10:11] nt
	s_add_u32 s10, s10, s27
	s_addc_u32 s11, s11, 0
	global_load_dwordx4 v[72:75], v6, s[10:11] nt
	s_add_u32 s10, s10, s27
	s_addc_u32 s11, s11, 0
	global_load_dwordx4 v[76:79], v6, s[10:11] nt
	s_add_u32 s2, s2, s24
	s_addc_u32 s3, s3, 0
	s_add_u32 s2, s2, s22
	s_addc_u32 s3, s3, s23
	s_lshl_b32 s27, s14, 15
	s_add_u32 s2, s2, s27
	s_addc_u32 s3, s3, 0
	s_lshl_b32 s27, s12, 7
	s_add_u32 s2, s2, s27
	s_addc_u32 s3, s3, 0
	s_mov_b32 s28, 0x0f0f0f0f
	s_mov_b32 s29, 0x0f0f0f0f
	s_waitcnt vmcnt(0)
	s_mov_b64 exec, s[28:29]
	v_mul_f32_e32 v80, 0x42000000, v16
	v_mul_f32_e32 v81, 0x42000000, v17
	v_mul_f32_e32 v82, 0x42000000, v18
	v_mul_f32_e32 v83, 0x42000000, v19
	ds_write_b32 v7, v80 offset:0
	ds_write_b32 v7, v81 offset:4
	ds_write_b32 v7, v82 offset:8
	ds_write_b32 v7, v83 offset:12
	v_mul_f32_e32 v80, 0x42000000, v20
	v_mul_f32_e32 v81, 0x42000000, v21
	v_mul_f32_e32 v82, 0x42000000, v22
	v_mul_f32_e32 v83, 0x42000000, v23
	ds_write_b32 v7, v80 offset:544
	ds_write_b32 v7, v81 offset:548
	ds_write_b32 v7, v82 offset:552
	ds_write_b32 v7, v83 offset:556
	v_mul_f32_e32 v80, 0x42000000, v24
	v_mul_f32_e32 v81, 0x42000000, v25
	v_mul_f32_e32 v82, 0x42000000, v26
	v_mul_f32_e32 v83, 0x42000000, v27
	ds_write_b32 v7, v80 offset:1088
	ds_write_b32 v7, v81 offset:1092
	ds_write_b32 v7, v82 offset:1096
	ds_write_b32 v7, v83 offset:1100
	v_mul_f32_e32 v80, 0x42000000, v28
	v_mul_f32_e32 v81, 0x42000000, v29
	v_mul_f32_e32 v82, 0x42000000, v30
	v_mul_f32_e32 v83, 0x42000000, v31
	ds_write_b32 v7, v80 offset:1632
	ds_write_b32 v7, v81 offset:1636
	ds_write_b32 v7, v82 offset:1640
	ds_write_b32 v7, v83 offset:1644
	v_mul_f32_e32 v80, 0x42000000, v32
	v_mul_f32_e32 v81, 0x42000000, v33
	v_mul_f32_e32 v82, 0x42000000, v34
	v_mul_f32_e32 v83, 0x42000000, v35
	ds_write_b32 v7, v80 offset:2176
	ds_write_b32 v7, v81 offset:2180
	ds_write_b32 v7, v82 offset:2184
	ds_write_b32 v7, v83 offset:2188
	v_mul_f32_e32 v80, 0x42000000, v36
	v_mul_f32_e32 v81, 0x42000000, v37
	v_mul_f32_e32 v82, 0x42000000, v38
	v_mul_f32_e32 v83, 0x42000000, v39
	ds_write_b32 v7, v80 offset:2720
	ds_write_b32 v7, v81 offset:2724
	ds_write_b32 v7, v82 offset:2728
	ds_write_b32 v7, v83 offset:2732
	v_mul_f32_e32 v80, 0x42000000, v40
	v_mul_f32_e32 v81, 0x42000000, v41
	v_mul_f32_e32 v82, 0x42000000, v42
	v_mul_f32_e32 v83, 0x42000000, v43
	ds_write_b32 v7, v80 offset:3264
	ds_write_b32 v7, v81 offset:3268
	ds_write_b32 v7, v82 offset:3272
	ds_write_b32 v7, v83 offset:3276
	v_mul_f32_e32 v80, 0x42000000, v44
	v_mul_f32_e32 v81, 0x42000000, v45
	v_mul_f32_e32 v82, 0x42000000, v46
	v_mul_f32_e32 v83, 0x42000000, v47
	ds_write_b32 v7, v80 offset:3808
	ds_write_b32 v7, v81 offset:3812
	ds_write_b32 v7, v82 offset:3816
	ds_write_b32 v7, v83 offset:3820
	v_mul_f32_e32 v80, 0x42000000, v48
	v_mul_f32_e32 v81, 0x42000000, v49
	v_mul_f32_e32 v82, 0x42000000, v50
	v_mul_f32_e32 v83, 0x42000000, v51
	ds_write_b32 v7, v80 offset:4352
	ds_write_b32 v7, v81 offset:4356
	ds_write_b32 v7, v82 offset:4360
	ds_write_b32 v7, v83 offset:4364
	v_mul_f32_e32 v80, 0x42000000, v52
	v_mul_f32_e32 v81, 0x42000000, v53
	v_mul_f32_e32 v82, 0x42000000, v54
	v_mul_f32_e32 v83, 0x42000000, v55
	ds_write_b32 v7, v80 offset:4896
	ds_write_b32 v7, v81 offset:4900
	ds_write_b32 v7, v82 offset:4904
	ds_write_b32 v7, v83 offset:4908
	v_mul_f32_e32 v80, 0x42000000, v56
	v_mul_f32_e32 v81, 0x42000000, v57
	v_mul_f32_e32 v82, 0x42000000, v58
	v_mul_f32_e32 v83, 0x42000000, v59
	ds_write_b32 v7, v80 offset:5440
	ds_write_b32 v7, v81 offset:5444
	ds_write_b32 v7, v82 offset:5448
	ds_write_b32 v7, v83 offset:5452
	v_mul_f32_e32 v80, 0x42000000, v60
	v_mul_f32_e32 v81, 0x42000000, v61
	v_mul_f32_e32 v82, 0x42000000, v62
	v_mul_f32_e32 v83, 0x42000000, v63
	ds_write_b32 v7, v80 offset:5984
	ds_write_b32 v7, v81 offset:5988
	ds_write_b32 v7, v82 offset:5992
	ds_write_b32 v7, v83 offset:5996
	v_mul_f32_e32 v80, 0x42000000, v64
	v_mul_f32_e32 v81, 0x42000000, v65
	v_mul_f32_e32 v82, 0x42000000, v66
	v_mul_f32_e32 v83, 0x42000000, v67
	ds_write_b32 v7, v80 offset:6528
	ds_write_b32 v7, v81 offset:6532
	ds_write_b32 v7, v82 offset:6536
	ds_write_b32 v7, v83 offset:6540
	v_mul_f32_e32 v80, 0x42000000, v68
	v_mul_f32_e32 v81, 0x42000000, v69
	v_mul_f32_e32 v82, 0x42000000, v70
	v_mul_f32_e32 v83, 0x42000000, v71
	ds_write_b32 v7, v80 offset:7072
	ds_write_b32 v7, v81 offset:7076
	ds_write_b32 v7, v82 offset:7080
	ds_write_b32 v7, v83 offset:7084
	v_mul_f32_e32 v80, 0x42000000, v72
	v_mul_f32_e32 v81, 0x42000000, v73
	v_mul_f32_e32 v82, 0x42000000, v74
	v_mul_f32_e32 v83, 0x42000000, v75
	ds_write_b32 v7, v80 offset:7616
	ds_write_b32 v7, v81 offset:7620
	ds_write_b32 v7, v82 offset:7624
	ds_write_b32 v7, v83 offset:7628
	v_mul_f32_e32 v80, 0x42000000, v76
	v_mul_f32_e32 v81, 0x42000000, v77
	v_mul_f32_e32 v82, 0x42000000, v78
	v_mul_f32_e32 v83, 0x42000000, v79
	ds_write_b32 v7, v80 offset:8160
	ds_write_b32 v7, v81 offset:8164
	ds_write_b32 v7, v82 offset:8168
	ds_write_b32 v7, v83 offset:8172
	s_mov_b64 exec, -1
	s_waitcnt lgkmcnt(0)
	ds_read_b32 v84, v8 offset:0
	ds_read_b32 v85, v8 offset:68
	ds_read_b32 v86, v8 offset:136
	ds_read_b32 v87, v8 offset:204
	ds_read_b32 v88, v8 offset:272
	ds_read_b32 v89, v8 offset:340
	ds_read_b32 v90, v8 offset:408
	ds_read_b32 v91, v8 offset:476
	ds_read_b32 v92, v8 offset:544
	ds_read_b32 v93, v8 offset:612
	ds_read_b32 v94, v8 offset:680
	ds_read_b32 v95, v8 offset:748
	ds_read_b32 v96, v8 offset:816
	ds_read_b32 v97, v8 offset:884
	ds_read_b32 v98, v8 offset:952
	ds_read_b32 v99, v8 offset:1020
	s_waitcnt lgkmcnt(0)
	v_cvt_pk_fp8_f32 v100, v84, v85
	s_nop 0
	v_cvt_pk_fp8_f32 v100, v86, v87 op_sel:[0,0,1]
	v_cvt_pk_fp8_f32 v101, v88, v89
	s_nop 0
	v_cvt_pk_fp8_f32 v101, v90, v91 op_sel:[0,0,1]
	v_cvt_pk_fp8_f32 v102, v92, v93
	s_nop 0
	v_cvt_pk_fp8_f32 v102, v94, v95 op_sel:[0,0,1]
	v_cvt_pk_fp8_f32 v103, v96, v97
	s_nop 0
	v_cvt_pk_fp8_f32 v103, v98, v99 op_sel:[0,0,1]
	s_nop 0
	global_store_dwordx4 v9, v[100:103], s[2:3]
	s_nop 1
	ds_read_b32 v84, v8 offset:32
	ds_read_b32 v85, v8 offset:100
	ds_read_b32 v86, v8 offset:168
	ds_read_b32 v87, v8 offset:236
	ds_read_b32 v88, v8 offset:304
	ds_read_b32 v89, v8 offset:372
	ds_read_b32 v90, v8 offset:440
	ds_read_b32 v91, v8 offset:508
	ds_read_b32 v92, v8 offset:576
	ds_read_b32 v93, v8 offset:644
	ds_read_b32 v94, v8 offset:712
	ds_read_b32 v95, v8 offset:780
	ds_read_b32 v96, v8 offset:848
	ds_read_b32 v97, v8 offset:916
	ds_read_b32 v98, v8 offset:984
	ds_read_b32 v99, v8 offset:1052
	s_waitcnt lgkmcnt(0)
	v_cvt_pk_fp8_f32 v100, v84, v85
	s_nop 0
	v_cvt_pk_fp8_f32 v100, v86, v87 op_sel:[0,0,1]
	v_cvt_pk_fp8_f32 v101, v88, v89
	s_nop 0
	v_cvt_pk_fp8_f32 v101, v90, v91 op_sel:[0,0,1]
	v_cvt_pk_fp8_f32 v102, v92, v93
	s_nop 0
	v_cvt_pk_fp8_f32 v102, v94, v95 op_sel:[0,0,1]
	v_cvt_pk_fp8_f32 v103, v96, v97
	s_nop 0
	v_cvt_pk_fp8_f32 v103, v98, v99 op_sel:[0,0,1]
	s_nop 0
	global_store_dwordx4 v10, v[100:103], s[2:3]
	s_nop 1
	s_waitcnt lgkmcnt(0)
	s_not_b64 s[28:29], s[28:29]
	s_add_u32 s2, s2, 0x4000
	s_addc_u32 s3, s3, 0
	s_mov_b64 exec, s[28:29]
	v_mul_f32_e32 v80, 0x42000000, v16
	v_mul_f32_e32 v81, 0x42000000, v17
	v_mul_f32_e32 v82, 0x42000000, v18
	v_mul_f32_e32 v83, 0x42000000, v19
	ds_write_b32 v7, v80 offset:0
	ds_write_b32 v7, v81 offset:4
	ds_write_b32 v7, v82 offset:8
	ds_write_b32 v7, v83 offset:12
	v_mul_f32_e32 v80, 0x42000000, v20
	v_mul_f32_e32 v81, 0x42000000, v21
	v_mul_f32_e32 v82, 0x42000000, v22
	v_mul_f32_e32 v83, 0x42000000, v23
	ds_write_b32 v7, v80 offset:544
	ds_write_b32 v7, v81 offset:548
	ds_write_b32 v7, v82 offset:552
	ds_write_b32 v7, v83 offset:556
	v_mul_f32_e32 v80, 0x42000000, v24
	v_mul_f32_e32 v81, 0x42000000, v25
	v_mul_f32_e32 v82, 0x42000000, v26
	v_mul_f32_e32 v83, 0x42000000, v27
	ds_write_b32 v7, v80 offset:1088
	ds_write_b32 v7, v81 offset:1092
	ds_write_b32 v7, v82 offset:1096
	ds_write_b32 v7, v83 offset:1100
	v_mul_f32_e32 v80, 0x42000000, v28
	v_mul_f32_e32 v81, 0x42000000, v29
	v_mul_f32_e32 v82, 0x42000000, v30
	v_mul_f32_e32 v83, 0x42000000, v31
	ds_write_b32 v7, v80 offset:1632
	ds_write_b32 v7, v81 offset:1636
	ds_write_b32 v7, v82 offset:1640
	ds_write_b32 v7, v83 offset:1644
	v_mul_f32_e32 v80, 0x42000000, v32
	v_mul_f32_e32 v81, 0x42000000, v33
	v_mul_f32_e32 v82, 0x42000000, v34
	v_mul_f32_e32 v83, 0x42000000, v35
	ds_write_b32 v7, v80 offset:2176
	ds_write_b32 v7, v81 offset:2180
	ds_write_b32 v7, v82 offset:2184
	ds_write_b32 v7, v83 offset:2188
	v_mul_f32_e32 v80, 0x42000000, v36
	v_mul_f32_e32 v81, 0x42000000, v37
	v_mul_f32_e32 v82, 0x42000000, v38
	v_mul_f32_e32 v83, 0x42000000, v39
	ds_write_b32 v7, v80 offset:2720
	ds_write_b32 v7, v81 offset:2724
	ds_write_b32 v7, v82 offset:2728
	ds_write_b32 v7, v83 offset:2732
	v_mul_f32_e32 v80, 0x42000000, v40
	v_mul_f32_e32 v81, 0x42000000, v41
	v_mul_f32_e32 v82, 0x42000000, v42
	v_mul_f32_e32 v83, 0x42000000, v43
	ds_write_b32 v7, v80 offset:3264
	ds_write_b32 v7, v81 offset:3268
	ds_write_b32 v7, v82 offset:3272
	ds_write_b32 v7, v83 offset:3276
	v_mul_f32_e32 v80, 0x42000000, v44
	v_mul_f32_e32 v81, 0x42000000, v45
	v_mul_f32_e32 v82, 0x42000000, v46
	v_mul_f32_e32 v83, 0x42000000, v47
	ds_write_b32 v7, v80 offset:3808
	ds_write_b32 v7, v81 offset:3812
	ds_write_b32 v7, v82 offset:3816
	ds_write_b32 v7, v83 offset:3820
	v_mul_f32_e32 v80, 0x42000000, v48
	v_mul_f32_e32 v81, 0x42000000, v49
	v_mul_f32_e32 v82, 0x42000000, v50
	v_mul_f32_e32 v83, 0x42000000, v51
	ds_write_b32 v7, v80 offset:4352
	ds_write_b32 v7, v81 offset:4356
	ds_write_b32 v7, v82 offset:4360
	ds_write_b32 v7, v83 offset:4364
	v_mul_f32_e32 v80, 0x42000000, v52
	v_mul_f32_e32 v81, 0x42000000, v53
	v_mul_f32_e32 v82, 0x42000000, v54
	v_mul_f32_e32 v83, 0x42000000, v55
	ds_write_b32 v7, v80 offset:4896
	ds_write_b32 v7, v81 offset:4900
	ds_write_b32 v7, v82 offset:4904
	ds_write_b32 v7, v83 offset:4908
	v_mul_f32_e32 v80, 0x42000000, v56
	v_mul_f32_e32 v81, 0x42000000, v57
	v_mul_f32_e32 v82, 0x42000000, v58
	v_mul_f32_e32 v83, 0x42000000, v59
	ds_write_b32 v7, v80 offset:5440
	ds_write_b32 v7, v81 offset:5444
	ds_write_b32 v7, v82 offset:5448
	ds_write_b32 v7, v83 offset:5452
	v_mul_f32_e32 v80, 0x42000000, v60
	v_mul_f32_e32 v81, 0x42000000, v61
	v_mul_f32_e32 v82, 0x42000000, v62
	v_mul_f32_e32 v83, 0x42000000, v63
	ds_write_b32 v7, v80 offset:5984
	ds_write_b32 v7, v81 offset:5988
	ds_write_b32 v7, v82 offset:5992
	ds_write_b32 v7, v83 offset:5996
	v_mul_f32_e32 v80, 0x42000000, v64
	v_mul_f32_e32 v81, 0x42000000, v65
	v_mul_f32_e32 v82, 0x42000000, v66
	v_mul_f32_e32 v83, 0x42000000, v67
	ds_write_b32 v7, v80 offset:6528
	ds_write_b32 v7, v81 offset:6532
	ds_write_b32 v7, v82 offset:6536
	ds_write_b32 v7, v83 offset:6540
	v_mul_f32_e32 v80, 0x42000000, v68
	v_mul_f32_e32 v81, 0x42000000, v69
	v_mul_f32_e32 v82, 0x42000000, v70
	v_mul_f32_e32 v83, 0x42000000, v71
	ds_write_b32 v7, v80 offset:7072
	ds_write_b32 v7, v81 offset:7076
	ds_write_b32 v7, v82 offset:7080
	ds_write_b32 v7, v83 offset:7084
	v_mul_f32_e32 v80, 0x42000000, v72
	v_mul_f32_e32 v81, 0x42000000, v73
	v_mul_f32_e32 v82, 0x42000000, v74
	v_mul_f32_e32 v83, 0x42000000, v75
	ds_write_b32 v7, v80 offset:7616
	ds_write_b32 v7, v81 offset:7620
	ds_write_b32 v7, v82 offset:7624
	ds_write_b32 v7, v83 offset:7628
	v_mul_f32_e32 v80, 0x42000000, v76
	v_mul_f32_e32 v81, 0x42000000, v77
	v_mul_f32_e32 v82, 0x42000000, v78
	v_mul_f32_e32 v83, 0x42000000, v79
	ds_write_b32 v7, v80 offset:8160
	ds_write_b32 v7, v81 offset:8164
	ds_write_b32 v7, v82 offset:8168
	ds_write_b32 v7, v83 offset:8172
	s_mov_b64 exec, -1
	s_waitcnt lgkmcnt(0)
	ds_read_b32 v84, v8 offset:0
	ds_read_b32 v85, v8 offset:68
	ds_read_b32 v86, v8 offset:136
	ds_read_b32 v87, v8 offset:204
	ds_read_b32 v88, v8 offset:272
	ds_read_b32 v89, v8 offset:340
	ds_read_b32 v90, v8 offset:408
	ds_read_b32 v91, v8 offset:476
	ds_read_b32 v92, v8 offset:544
	ds_read_b32 v93, v8 offset:612
	ds_read_b32 v94, v8 offset:680
	ds_read_b32 v95, v8 offset:748
	ds_read_b32 v96, v8 offset:816
	ds_read_b32 v97, v8 offset:884
	ds_read_b32 v98, v8 offset:952
	ds_read_b32 v99, v8 offset:1020
	s_waitcnt lgkmcnt(0)
	v_cvt_pk_fp8_f32 v100, v84, v85
	s_nop 0
	v_cvt_pk_fp8_f32 v100, v86, v87 op_sel:[0,0,1]
	v_cvt_pk_fp8_f32 v101, v88, v89
	s_nop 0
	v_cvt_pk_fp8_f32 v101, v90, v91 op_sel:[0,0,1]
	v_cvt_pk_fp8_f32 v102, v92, v93
	s_nop 0
	v_cvt_pk_fp8_f32 v102, v94, v95 op_sel:[0,0,1]
	v_cvt_pk_fp8_f32 v103, v96, v97
	s_nop 0
	v_cvt_pk_fp8_f32 v103, v98, v99 op_sel:[0,0,1]
	s_nop 0
	global_store_dwordx4 v9, v[100:103], s[2:3]
	s_nop 1
	ds_read_b32 v84, v8 offset:32
	ds_read_b32 v85, v8 offset:100
	ds_read_b32 v86, v8 offset:168
	ds_read_b32 v87, v8 offset:236
	ds_read_b32 v88, v8 offset:304
	ds_read_b32 v89, v8 offset:372
	ds_read_b32 v90, v8 offset:440
	ds_read_b32 v91, v8 offset:508
	ds_read_b32 v92, v8 offset:576
	ds_read_b32 v93, v8 offset:644
	ds_read_b32 v94, v8 offset:712
	ds_read_b32 v95, v8 offset:780
	ds_read_b32 v96, v8 offset:848
	ds_read_b32 v97, v8 offset:916
	ds_read_b32 v98, v8 offset:984
	ds_read_b32 v99, v8 offset:1052
	s_waitcnt lgkmcnt(0)
	v_cvt_pk_fp8_f32 v100, v84, v85
	s_nop 0
	v_cvt_pk_fp8_f32 v100, v86, v87 op_sel:[0,0,1]
	v_cvt_pk_fp8_f32 v101, v88, v89
	s_nop 0
	v_cvt_pk_fp8_f32 v101, v90, v91 op_sel:[0,0,1]
	v_cvt_pk_fp8_f32 v102, v92, v93
	s_nop 0
	v_cvt_pk_fp8_f32 v102, v94, v95 op_sel:[0,0,1]
	v_cvt_pk_fp8_f32 v103, v96, v97
	s_nop 0
	v_cvt_pk_fp8_f32 v103, v98, v99 op_sel:[0,0,1]
	s_nop 0
	global_store_dwordx4 v10, v[100:103], s[2:3]
	s_nop 1
.Lcvtw_ret:
	s_mov_b64 exec, -1
	s_cmp_eq_u32 s31, 0
	s_cbranch_scc1 .LBB0_326
	s_cmp_eq_u32 s31, 1
	s_cbranch_scc1 .LBB0_404
	s_cmp_eq_u32 s31, 2
	s_cbranch_scc1 .LBB0_533
	s_cmp_eq_u32 s31, 3
	s_cbranch_scc1 .LBB0_610
	s_cmp_eq_u32 s31, 4
	s_cbranch_scc1 .LBB0_673
	s_cmp_eq_u32 s31, 5
	s_cbranch_scc1 .LBB0_849
	s_cmp_eq_u32 s31, 6
	s_cbranch_scc1 .LBB0_955
	s_cmp_eq_u32 s31, 7
	s_cbranch_scc1 .LBB0_1074
	s_cmp_eq_u32 s31, 8
	s_cbranch_scc1 .LBB0_1171
	s_cmp_eq_u32 s31, 9
	s_cbranch_scc1 .LBB0_1342
	s_cmp_eq_u32 s31, 10
	s_cbranch_scc1 .LBB0_245
	s_cmp_eq_u32 s31, 11
	s_cbranch_scc1 .LBB0_242
	s_branch .LBB0_326

.LBB0_1383:
	s_waitcnt vmcnt(0)
	s_waitcnt vmcnt(0)
	s_barrier
	s_mov_b64 s[2:3], exec
	s_load_dword s92, s[0:1], 0x110
	v_readlane_b32 s4, v255, 6
	v_readlane_b32 s5, v255, 7
	s_and_b64 s[4:5], s[2:3], s[4:5]
	s_xor_b64 s[2:3], s[4:5], s[2:3]
	s_mov_b32 s44, 0x80000
	s_movk_i32 s45, 0xff7c
	s_mov_b64 exec, s[4:5]
	s_cbranch_execz .Lcvt_site_10
	s_cbranch_execnz .LBB0_1384
	s_getpc_b64 s[98:99]
